# plus: G1/M1 K-loop load segments issue B and A fragment reads as one burst (no lgkmcnt(0) between the groups)
# speedup vs baseline: 1.0099x; 1.0099x over previous
.LBB0_514:
	s_add_u32 s22, s82, s92
	s_addc_u32 s23, s83, s93
	s_add_u32 s24, s22, 0x100
	s_addc_u32 s25, s23, 0
	s_add_u32 s58, s3, s92
	s_addc_u32 s59, s2, s93
	s_add_i32 vcc_lo, 0, 0x10000
	s_cmpk_eq_i32 s92, 0xf00
	s_cselect_b64 s[26:27], -1, 0
	s_and_b64 s[22:23], s[26:27], exec
	s_cselect_b32 s25, s67, s25
	s_cselect_b32 s24, s75, s24
	s_cselect_b32 s23, s95, s59
	s_cselect_b32 s22, s29, s58
	s_add_i32 vcc_hi, 0, 0x14000
	v_add_u32_e32 v130, vcc_lo, v223
	v_add_u32_e32 v142, vcc_hi, v223
	ds_read_b128 v[146:149], v130
	ds_read_b128 v[150:153], v130 offset:1024
	ds_read_b128 v[154:157], v130 offset:2048
	ds_read_b128 v[158:161], v130 offset:3072
	ds_read_b128 v[130:133], v142
	ds_read_b128 v[134:137], v142 offset:1024
	ds_read_b128 v[138:141], v142 offset:2048
	ds_read_b128 v[142:145], v142 offset:3072
	v_lshl_add_u64 v[214:215], v[210:211], 0, s[92:93]
	s_add_i32 m0, s81, 0xc000
	ds_read_b128 v[162:165], v224
	ds_read_b128 v[166:169], v224 offset:1024
	ds_read_b128 v[170:173], v224 offset:2048
	ds_read_b128 v[174:177], v224 offset:3072
	ds_read_b128 v[178:181], v224 offset:4096
	ds_read_b128 v[182:185], v224 offset:5120
	ds_read_b128 v[186:189], v224 offset:6144
	ds_read_b128 v[190:193], v224 offset:7168
	global_load_lds_dwordx4 v[214:215], off
	v_lshl_add_u64 v[214:215], v[212:213], 0, s[92:93]
	s_add_i32 m0, s81, 0xe000
	s_nop 0
	global_load_lds_dwordx4 v[214:215], off
	s_waitcnt vmcnt(8)
	s_waitcnt lgkmcnt(0)
	s_barrier
	v_mfma_f32_16x16x32_bf16 v[124:127], v[146:149], v[162:165], v[124:127]
	v_mfma_f32_16x16x32_bf16 v[120:123], v[154:157], v[162:165], v[120:123]
	v_mfma_f32_16x16x32_bf16 v[116:119], v[146:149], v[170:173], v[116:119]
	v_mfma_f32_16x16x32_bf16 v[108:111], v[154:157], v[170:173], v[108:111]
	v_mfma_f32_16x16x32_bf16 v[100:103], v[146:149], v[178:181], v[100:103]
	v_mfma_f32_16x16x32_bf16 v[92:95], v[154:157], v[178:181], v[92:95]
	v_mfma_f32_16x16x32_bf16 v[84:87], v[146:149], v[186:189], v[84:87]
	v_mfma_f32_16x16x32_bf16 v[76:79], v[154:157], v[186:189], v[76:79]
	v_mfma_f32_16x16x32_bf16 v[124:127], v[150:153], v[166:169], v[124:127]
	v_mfma_f32_16x16x32_bf16 v[120:123], v[158:161], v[166:169], v[120:123]
	v_mfma_f32_16x16x32_bf16 v[116:119], v[150:153], v[174:177], v[116:119]
	v_mfma_f32_16x16x32_bf16 v[108:111], v[158:161], v[174:177], v[108:111]
	v_mfma_f32_16x16x32_bf16 v[100:103], v[150:153], v[182:185], v[100:103]
	v_mfma_f32_16x16x32_bf16 v[92:95], v[158:161], v[182:185], v[92:95]
	v_mfma_f32_16x16x32_bf16 v[84:87], v[150:153], v[190:193], v[84:87]
	v_mfma_f32_16x16x32_bf16 v[76:79], v[158:161], v[190:193], v[76:79]
	v_mfma_f32_16x16x32_bf16 v[112:115], v[130:133], v[162:165], v[112:115]
	v_mfma_f32_16x16x32_bf16 v[104:107], v[138:141], v[162:165], v[104:107]
	v_mfma_f32_16x16x32_bf16 v[96:99], v[130:133], v[170:173], v[96:99]
	v_mfma_f32_16x16x32_bf16 v[88:91], v[138:141], v[170:173], v[88:91]
	v_mfma_f32_16x16x32_bf16 v[80:83], v[130:133], v[178:181], v[80:83]
	v_mfma_f32_16x16x32_bf16 v[72:75], v[138:141], v[178:181], v[72:75]
	v_mfma_f32_16x16x32_bf16 v[68:71], v[130:133], v[186:189], v[68:71]
	v_mfma_f32_16x16x32_bf16 v[64:67], v[138:141], v[186:189], v[64:67]
	v_mfma_f32_16x16x32_bf16 v[112:115], v[134:137], v[166:169], v[112:115]
	v_mfma_f32_16x16x32_bf16 v[104:107], v[142:145], v[166:169], v[104:107]
	v_mfma_f32_16x16x32_bf16 v[96:99], v[134:137], v[174:177], v[96:99]
	v_mfma_f32_16x16x32_bf16 v[88:91], v[142:145], v[174:177], v[88:91]
	v_mfma_f32_16x16x32_bf16 v[80:83], v[134:137], v[182:185], v[80:83]
	v_mfma_f32_16x16x32_bf16 v[72:75], v[142:145], v[182:185], v[72:75]
	v_mfma_f32_16x16x32_bf16 v[68:71], v[134:137], v[190:193], v[68:71]
	v_mfma_f32_16x16x32_bf16 v[64:67], v[142:145], v[190:193], v[64:67]
	s_barrier
	s_add_i32 s58, vcc_lo, s28
	v_lshl_add_u64 v[214:215], s[22:23], 0, v[200:201]
	s_mov_b32 m0, s58
	ds_read_b128 v[186:189], v224 offset:16384
	ds_read_b128 v[190:193], v224 offset:17408
	ds_read_b128 v[178:181], v224 offset:18432
	ds_read_b128 v[182:185], v224 offset:19456
	ds_read_b128 v[170:173], v224 offset:20480
	ds_read_b128 v[174:177], v224 offset:21504
	ds_read_b128 v[162:165], v224 offset:22528
	ds_read_b128 v[166:169], v224 offset:23552
	global_load_lds_dwordx4 v[214:215], off
	s_add_i32 m0, s58, 0x2000
	s_add_u32 s58, s22, 0x80000
	v_lshl_add_u64 v[216:217], s[22:23], 0, v[204:205]
	s_addc_u32 s59, s23, 0
	s_add_i32 vcc_lo, vcc_hi, s28
	global_load_lds_dwordx4 v[216:217], off
	v_lshl_add_u64 v[218:219], s[58:59], 0, v[200:201]
	s_mov_b32 m0, vcc_lo
	v_lshl_add_u64 v[220:221], s[24:25], 0, v[202:203]
	global_load_lds_dwordx4 v[218:219], off
	v_lshl_add_u64 v[218:219], s[58:59], 0, v[204:205]
	s_add_i32 m0, vcc_lo, 0x2000
	v_cndmask_b32_e64 v194, 0, 1, s[96:97]
	global_load_lds_dwordx4 v[218:219], off
	v_lshl_add_u64 v[218:219], s[24:25], 0, v[198:199]
	s_mov_b32 m0, s81
	v_cmp_ne_u32_e64 s[58:59], 1, v194
	global_load_lds_dwordx4 v[218:219], off
	s_mov_b32 m0, s88
	s_andn2_b64 vcc, exec, s[96:97]
	global_load_lds_dwordx4 v[220:221], off
	s_waitcnt vmcnt(8)
	s_waitcnt lgkmcnt(0)
	s_barrier
	s_cbranch_vccnz .LBB0_516
	s_waitcnt lgkmcnt(0)
	v_mfma_f32_16x16x32_bf16 v[60:63], v[146:149], v[186:189], v[60:63]
	v_mfma_f32_16x16x32_bf16 v[56:59], v[154:157], v[186:189], v[56:59]
	v_mfma_f32_16x16x32_bf16 v[44:47], v[146:149], v[178:181], v[44:47]
	v_mfma_f32_16x16x32_bf16 v[40:43], v[154:157], v[178:181], v[40:43]
	v_mfma_f32_16x16x32_bf16 v[28:31], v[146:149], v[170:173], v[28:31]
	v_mfma_f32_16x16x32_bf16 v[24:27], v[154:157], v[170:173], v[24:27]
	v_mfma_f32_16x16x32_bf16 v[12:15], v[146:149], v[162:165], v[12:15]
	v_mfma_f32_16x16x32_bf16 v[8:11], v[154:157], v[162:165], v[8:11]
	v_mfma_f32_16x16x32_bf16 v[60:63], v[150:153], v[190:193], v[60:63]
	v_mfma_f32_16x16x32_bf16 v[56:59], v[158:161], v[190:193], v[56:59]
	v_mfma_f32_16x16x32_bf16 v[44:47], v[150:153], v[182:185], v[44:47]
	v_mfma_f32_16x16x32_bf16 v[40:43], v[158:161], v[182:185], v[40:43]
	v_mfma_f32_16x16x32_bf16 v[28:31], v[150:153], v[174:177], v[28:31]
	v_mfma_f32_16x16x32_bf16 v[24:27], v[158:161], v[174:177], v[24:27]
	v_mfma_f32_16x16x32_bf16 v[12:15], v[150:153], v[166:169], v[12:15]
	v_mfma_f32_16x16x32_bf16 v[8:11], v[158:161], v[166:169], v[8:11]
	v_mfma_f32_16x16x32_bf16 v[52:55], v[130:133], v[186:189], v[52:55]
	v_mfma_f32_16x16x32_bf16 v[48:51], v[138:141], v[186:189], v[48:51]
	v_mfma_f32_16x16x32_bf16 v[36:39], v[130:133], v[178:181], v[36:39]
	v_mfma_f32_16x16x32_bf16 v[32:35], v[138:141], v[178:181], v[32:35]
	v_mfma_f32_16x16x32_bf16 v[20:23], v[130:133], v[170:173], v[20:23]
	v_mfma_f32_16x16x32_bf16 v[16:19], v[138:141], v[170:173], v[16:19]
	v_mfma_f32_16x16x32_bf16 v[4:7], v[130:133], v[162:165], v[4:7]
	v_mfma_f32_16x16x32_bf16 v[0:3], v[138:141], v[162:165], v[0:3]
	v_mfma_f32_16x16x32_bf16 v[52:55], v[134:137], v[190:193], v[52:55]
	v_mfma_f32_16x16x32_bf16 v[48:51], v[142:145], v[190:193], v[48:51]
	v_mfma_f32_16x16x32_bf16 v[36:39], v[134:137], v[182:185], v[36:39]
	v_mfma_f32_16x16x32_bf16 v[32:35], v[142:145], v[182:185], v[32:35]
	v_mfma_f32_16x16x32_bf16 v[20:23], v[134:137], v[174:177], v[20:23]
	v_mfma_f32_16x16x32_bf16 v[16:19], v[142:145], v[174:177], v[16:19]
	v_mfma_f32_16x16x32_bf16 v[4:7], v[134:137], v[166:169], v[4:7]
	v_mfma_f32_16x16x32_bf16 v[0:3], v[142:145], v[166:169], v[0:3]
.LBB0_516:
	s_barrier
	s_add_i32 vcc_lo, 0, 0x18000
	s_add_i32 vcc_hi, 0, 0x1c000
	v_add_u32_e32 v130, vcc_lo, v223
	v_add_u32_e32 v142, vcc_hi, v223
	ds_read_b128 v[146:149], v130
	ds_read_b128 v[150:153], v130 offset:1024
	ds_read_b128 v[154:157], v130 offset:2048
	ds_read_b128 v[158:161], v130 offset:3072
	ds_read_b128 v[130:133], v142
	ds_read_b128 v[134:137], v142 offset:1024
	ds_read_b128 v[138:141], v142 offset:2048
	ds_read_b128 v[142:145], v142 offset:3072
	s_and_b64 s[26:27], s[26:27], exec
	s_cselect_b32 s27, s72, s86
	s_cselect_b32 s26, 0, s87
	s_add_u32 s24, s24, s27
	s_addc_u32 s25, s25, s26
	s_mov_b32 m0, s89
	v_lshl_add_u64 v[226:227], s[24:25], 0, v[198:199]
	ds_read_b128 v[162:165], v224 offset:32768
	ds_read_b128 v[166:169], v224 offset:33792
	ds_read_b128 v[170:173], v224 offset:34816
	ds_read_b128 v[174:177], v224 offset:35840
	ds_read_b128 v[178:181], v224 offset:36864
	ds_read_b128 v[182:185], v224 offset:37888
	ds_read_b128 v[186:189], v224 offset:38912
	ds_read_b128 v[190:193], v224 offset:39936
	global_load_lds_dwordx4 v[226:227], off
	v_lshl_add_u64 v[226:227], s[24:25], 0, v[202:203]
	s_mov_b32 m0, s90
	s_nop 0
	global_load_lds_dwordx4 v[226:227], off
	s_waitcnt vmcnt(8)
	s_waitcnt lgkmcnt(0)
	s_barrier
	v_mfma_f32_16x16x32_bf16 v[124:127], v[146:149], v[162:165], v[124:127]
	v_mfma_f32_16x16x32_bf16 v[120:123], v[154:157], v[162:165], v[120:123]
	v_mfma_f32_16x16x32_bf16 v[116:119], v[146:149], v[170:173], v[116:119]
	v_mfma_f32_16x16x32_bf16 v[108:111], v[154:157], v[170:173], v[108:111]
	v_mfma_f32_16x16x32_bf16 v[100:103], v[146:149], v[178:181], v[100:103]
	v_mfma_f32_16x16x32_bf16 v[92:95], v[154:157], v[178:181], v[92:95]
	v_mfma_f32_16x16x32_bf16 v[84:87], v[146:149], v[186:189], v[84:87]
	v_mfma_f32_16x16x32_bf16 v[76:79], v[154:157], v[186:189], v[76:79]
	v_mfma_f32_16x16x32_bf16 v[124:127], v[150:153], v[166:169], v[124:127]
	v_mfma_f32_16x16x32_bf16 v[120:123], v[158:161], v[166:169], v[120:123]
	v_mfma_f32_16x16x32_bf16 v[116:119], v[150:153], v[174:177], v[116:119]
	v_mfma_f32_16x16x32_bf16 v[108:111], v[158:161], v[174:177], v[108:111]
	v_mfma_f32_16x16x32_bf16 v[100:103], v[150:153], v[182:185], v[100:103]
	v_mfma_f32_16x16x32_bf16 v[92:95], v[158:161], v[182:185], v[92:95]
	v_mfma_f32_16x16x32_bf16 v[84:87], v[150:153], v[190:193], v[84:87]
	v_mfma_f32_16x16x32_bf16 v[76:79], v[158:161], v[190:193], v[76:79]
	v_mfma_f32_16x16x32_bf16 v[112:115], v[130:133], v[162:165], v[112:115]
	v_mfma_f32_16x16x32_bf16 v[104:107], v[138:141], v[162:165], v[104:107]
	v_mfma_f32_16x16x32_bf16 v[96:99], v[130:133], v[170:173], v[96:99]
	v_mfma_f32_16x16x32_bf16 v[88:91], v[138:141], v[170:173], v[88:91]
	v_mfma_f32_16x16x32_bf16 v[80:83], v[130:133], v[178:181], v[80:83]
	v_mfma_f32_16x16x32_bf16 v[72:75], v[138:141], v[178:181], v[72:75]
	v_mfma_f32_16x16x32_bf16 v[68:71], v[130:133], v[186:189], v[68:71]
	v_mfma_f32_16x16x32_bf16 v[64:67], v[138:141], v[186:189], v[64:67]
	v_mfma_f32_16x16x32_bf16 v[112:115], v[134:137], v[166:169], v[112:115]
	v_mfma_f32_16x16x32_bf16 v[104:107], v[142:145], v[166:169], v[104:107]
	v_mfma_f32_16x16x32_bf16 v[96:99], v[134:137], v[174:177], v[96:99]
	v_mfma_f32_16x16x32_bf16 v[88:91], v[142:145], v[174:177], v[88:91]
	v_mfma_f32_16x16x32_bf16 v[80:83], v[134:137], v[182:185], v[80:83]
	v_mfma_f32_16x16x32_bf16 v[72:75], v[142:145], v[182:185], v[72:75]
	v_mfma_f32_16x16x32_bf16 v[68:71], v[134:137], v[190:193], v[68:71]
	v_mfma_f32_16x16x32_bf16 v[64:67], v[142:145], v[190:193], v[64:67]
	s_barrier
	s_add_i32 s24, vcc_lo, s28
	v_lshl_add_u64 v[214:215], v[214:215], 0, s[42:43]
	s_mov_b32 m0, s24
	ds_read_b128 v[186:189], v224 offset:49152
	ds_read_b128 v[190:193], v224 offset:50176
	ds_read_b128 v[178:181], v224 offset:51200
	ds_read_b128 v[182:185], v224 offset:52224
	ds_read_b128 v[170:173], v224 offset:53248
	ds_read_b128 v[174:177], v224 offset:54272
	ds_read_b128 v[162:165], v224 offset:55296
	ds_read_b128 v[166:169], v224 offset:56320
	global_load_lds_dwordx4 v[214:215], off
	s_add_i32 m0, s24, 0x2000
	s_add_u32 s22, s22, 0x80080
	v_lshl_add_u64 v[214:215], v[216:217], 0, s[42:43]
	s_addc_u32 s23, s23, 0
	s_add_i32 s24, vcc_hi, s28
	global_load_lds_dwordx4 v[214:215], off
	v_lshl_add_u64 v[214:215], s[22:23], 0, v[200:201]
	s_mov_b32 m0, s24
	s_and_b64 vcc, exec, s[58:59]
	global_load_lds_dwordx4 v[214:215], off
	v_lshl_add_u64 v[214:215], s[22:23], 0, v[204:205]
	s_add_i32 m0, s24, 0x2000
	s_nop 0
	global_load_lds_dwordx4 v[214:215], off
	v_lshl_add_u64 v[214:215], v[218:219], 0, s[42:43]
	s_mov_b32 m0, s91
	s_nop 0
	global_load_lds_dwordx4 v[214:215], off
	v_lshl_add_u64 v[214:215], v[220:221], 0, s[42:43]
	s_mov_b32 m0, s94
	s_nop 0
	global_load_lds_dwordx4 v[214:215], off
	s_waitcnt vmcnt(8)
	s_waitcnt lgkmcnt(0)
	s_barrier
	s_cbranch_vccnz .LBB0_513
	s_waitcnt lgkmcnt(0)
	v_mfma_f32_16x16x32_bf16 v[60:63], v[146:149], v[186:189], v[60:63]
	v_mfma_f32_16x16x32_bf16 v[56:59], v[154:157], v[186:189], v[56:59]
	v_mfma_f32_16x16x32_bf16 v[44:47], v[146:149], v[178:181], v[44:47]
	v_mfma_f32_16x16x32_bf16 v[40:43], v[154:157], v[178:181], v[40:43]
	v_mfma_f32_16x16x32_bf16 v[28:31], v[146:149], v[170:173], v[28:31]
	v_mfma_f32_16x16x32_bf16 v[24:27], v[154:157], v[170:173], v[24:27]
	v_mfma_f32_16x16x32_bf16 v[12:15], v[146:149], v[162:165], v[12:15]
	v_mfma_f32_16x16x32_bf16 v[8:11], v[154:157], v[162:165], v[8:11]
	v_mfma_f32_16x16x32_bf16 v[60:63], v[150:153], v[190:193], v[60:63]
	v_mfma_f32_16x16x32_bf16 v[56:59], v[158:161], v[190:193], v[56:59]
	v_mfma_f32_16x16x32_bf16 v[44:47], v[150:153], v[182:185], v[44:47]
	v_mfma_f32_16x16x32_bf16 v[40:43], v[158:161], v[182:185], v[40:43]
	v_mfma_f32_16x16x32_bf16 v[28:31], v[150:153], v[174:177], v[28:31]
	v_mfma_f32_16x16x32_bf16 v[24:27], v[158:161], v[174:177], v[24:27]
	v_mfma_f32_16x16x32_bf16 v[12:15], v[150:153], v[166:169], v[12:15]
	v_mfma_f32_16x16x32_bf16 v[8:11], v[158:161], v[166:169], v[8:11]
	v_mfma_f32_16x16x32_bf16 v[52:55], v[130:133], v[186:189], v[52:55]
	v_mfma_f32_16x16x32_bf16 v[48:51], v[138:141], v[186:189], v[48:51]
	v_mfma_f32_16x16x32_bf16 v[36:39], v[130:133], v[178:181], v[36:39]
	v_mfma_f32_16x16x32_bf16 v[32:35], v[138:141], v[178:181], v[32:35]
	v_mfma_f32_16x16x32_bf16 v[20:23], v[130:133], v[170:173], v[20:23]
	v_mfma_f32_16x16x32_bf16 v[16:19], v[138:141], v[170:173], v[16:19]
	v_mfma_f32_16x16x32_bf16 v[4:7], v[130:133], v[162:165], v[4:7]
	v_mfma_f32_16x16x32_bf16 v[0:3], v[138:141], v[162:165], v[0:3]
	v_mfma_f32_16x16x32_bf16 v[52:55], v[134:137], v[190:193], v[52:55]
	v_mfma_f32_16x16x32_bf16 v[48:51], v[142:145], v[190:193], v[48:51]
	v_mfma_f32_16x16x32_bf16 v[36:39], v[134:137], v[182:185], v[36:39]
	v_mfma_f32_16x16x32_bf16 v[32:35], v[142:145], v[182:185], v[32:35]
	v_mfma_f32_16x16x32_bf16 v[20:23], v[134:137], v[174:177], v[20:23]
	v_mfma_f32_16x16x32_bf16 v[16:19], v[142:145], v[174:177], v[16:19]
	v_mfma_f32_16x16x32_bf16 v[4:7], v[134:137], v[166:169], v[4:7]
	v_mfma_f32_16x16x32_bf16 v[0:3], v[142:145], v[166:169], v[0:3]
	s_branch .LBB0_513

.LBB0_1400:
	s_add_u32 s2, s64, s74
	s_addc_u32 s3, s65, s75
	s_add_u32 s22, s2, 0x28c00100
	s_addc_u32 s23, s3, 0
	s_cmpk_eq_i32 s74, 0xf00
	s_cselect_b64 s[60:61], -1, 0
	s_and_b64 s[2:3], s[60:61], exec
	s_cselect_b32 s23, s9, s23
	s_cselect_b32 s22, s8, s22
	v_add_u32_e32 v128, s26, v242
	s_add_i32 s2, 0, 0x14000
	v_lshl_add_u64 v[146:147], v[220:221], 0, s[74:75]
	ds_read_b128 v[130:133], v128
	ds_read_b128 v[134:137], v128 offset:1024
	ds_read_b128 v[138:141], v128 offset:2048
	ds_read_b128 v[142:145], v128 offset:3072
	v_add_u32_e32 v128, s2, v242
	v_cndmask_b32_e64 v223, v147, v207, s[60:61]
	v_cndmask_b32_e64 v222, v146, v206, s[60:61]
	ds_read_b128 v[146:149], v128
	ds_read_b128 v[150:153], v128 offset:1024
	ds_read_b128 v[154:157], v128 offset:2048
	ds_read_b128 v[158:161], v128 offset:3072
	v_lshl_add_u64 v[194:195], v[218:219], 0, s[74:75]
	s_add_i32 m0, s36, 0xc000
	ds_read_b128 v[162:165], v209
	ds_read_b128 v[166:169], v209 offset:1024
	ds_read_b128 v[170:173], v209 offset:2048
	ds_read_b128 v[174:177], v209 offset:3072
	ds_read_b128 v[178:181], v209 offset:4096
	ds_read_b128 v[182:185], v209 offset:5120
	ds_read_b128 v[186:189], v209 offset:6144
	ds_read_b128 v[190:193], v209 offset:7168
	global_load_lds_dwordx4 v[194:195], off
	v_lshl_add_u64 v[194:195], v[216:217], 0, s[74:75]
	s_add_i32 m0, s36, 0xe000
	s_nop 0
	global_load_lds_dwordx4 v[194:195], off
	s_waitcnt vmcnt(8)
	s_waitcnt lgkmcnt(0)
	s_barrier
	v_mfma_f32_16x16x32_bf16 v[124:127], v[130:133], v[162:165], v[124:127]
	v_mfma_f32_16x16x32_bf16 v[120:123], v[138:141], v[162:165], v[120:123]
	v_mfma_f32_16x16x32_bf16 v[108:111], v[130:133], v[170:173], v[108:111]
	v_mfma_f32_16x16x32_bf16 v[104:107], v[138:141], v[170:173], v[104:107]
	v_mfma_f32_16x16x32_bf16 v[92:95], v[130:133], v[178:181], v[92:95]
	v_mfma_f32_16x16x32_bf16 v[88:91], v[138:141], v[178:181], v[88:91]
	v_mfma_f32_16x16x32_bf16 v[76:79], v[130:133], v[186:189], v[76:79]
	v_mfma_f32_16x16x32_bf16 v[72:75], v[138:141], v[186:189], v[72:75]
	v_mfma_f32_16x16x32_bf16 v[124:127], v[134:137], v[166:169], v[124:127]
	v_mfma_f32_16x16x32_bf16 v[120:123], v[142:145], v[166:169], v[120:123]
	v_mfma_f32_16x16x32_bf16 v[108:111], v[134:137], v[174:177], v[108:111]
	v_mfma_f32_16x16x32_bf16 v[104:107], v[142:145], v[174:177], v[104:107]
	v_mfma_f32_16x16x32_bf16 v[92:95], v[134:137], v[182:185], v[92:95]
	v_mfma_f32_16x16x32_bf16 v[88:91], v[142:145], v[182:185], v[88:91]
	v_mfma_f32_16x16x32_bf16 v[76:79], v[134:137], v[190:193], v[76:79]
	v_mfma_f32_16x16x32_bf16 v[72:75], v[142:145], v[190:193], v[72:75]
	v_mfma_f32_16x16x32_bf16 v[116:119], v[146:149], v[162:165], v[116:119]
	v_mfma_f32_16x16x32_bf16 v[112:115], v[154:157], v[162:165], v[112:115]
	v_mfma_f32_16x16x32_bf16 v[100:103], v[146:149], v[170:173], v[100:103]
	v_mfma_f32_16x16x32_bf16 v[96:99], v[154:157], v[170:173], v[96:99]
	v_mfma_f32_16x16x32_bf16 v[84:87], v[146:149], v[178:181], v[84:87]
	v_mfma_f32_16x16x32_bf16 v[80:83], v[154:157], v[178:181], v[80:83]
	v_mfma_f32_16x16x32_bf16 v[68:71], v[146:149], v[186:189], v[68:71]
	v_mfma_f32_16x16x32_bf16 v[64:67], v[154:157], v[186:189], v[64:67]
	v_mfma_f32_16x16x32_bf16 v[116:119], v[150:153], v[166:169], v[116:119]
	v_mfma_f32_16x16x32_bf16 v[112:115], v[158:161], v[166:169], v[112:115]
	v_mfma_f32_16x16x32_bf16 v[100:103], v[150:153], v[174:177], v[100:103]
	v_mfma_f32_16x16x32_bf16 v[96:99], v[158:161], v[174:177], v[96:99]
	v_mfma_f32_16x16x32_bf16 v[84:87], v[150:153], v[182:185], v[84:87]
	v_mfma_f32_16x16x32_bf16 v[80:83], v[158:161], v[182:185], v[80:83]
	v_mfma_f32_16x16x32_bf16 v[68:71], v[150:153], v[190:193], v[68:71]
	v_mfma_f32_16x16x32_bf16 v[64:67], v[158:161], v[190:193], v[64:67]
	s_barrier
	s_add_i32 s3, s26, s33
	v_lshl_add_u64 v[224:225], v[222:223], 0, v[198:199]
	s_mov_b32 m0, s3
	ds_read_b128 v[186:189], v209 offset:16384
	ds_read_b128 v[190:193], v209 offset:17408
	ds_read_b128 v[178:181], v209 offset:18432
	ds_read_b128 v[182:185], v209 offset:19456
	ds_read_b128 v[170:173], v209 offset:20480
	ds_read_b128 v[174:177], v209 offset:21504
	ds_read_b128 v[162:165], v209 offset:22528
	ds_read_b128 v[166:169], v209 offset:23552
	global_load_lds_dwordx4 v[224:225], off
	v_lshl_add_u64 v[226:227], v[222:223], 0, v[200:201]
	s_add_i32 m0, s3, 0x2000
	v_lshl_add_u64 v[194:195], v[222:223], 0, s[40:41]
	s_add_i32 s2, s2, s33
	global_load_lds_dwordx4 v[226:227], off
	v_lshl_add_u64 v[196:197], v[194:195], 0, v[198:199]
	s_mov_b32 m0, s2
	v_lshl_add_u64 v[194:195], v[194:195], 0, v[200:201]
	global_load_lds_dwordx4 v[196:197], off
	s_add_i32 m0, s2, 0x2000
	v_cndmask_b32_e64 v128, v208, v211, s[60:61]
	global_load_lds_dwordx4 v[194:195], off
	s_mov_b32 m0, s36
	v_cndmask_b32_e64 v228, v210, v243, s[60:61]
	global_load_lds_dwordx4 v128, s[22:23]
	s_mov_b32 m0, s37
	v_cndmask_b32_e64 v194, 0, 1, s[20:21]
	global_load_lds_dwordx4 v228, s[22:23]
	s_waitcnt vmcnt(8)
	s_waitcnt lgkmcnt(0)
	v_cmp_ne_u32_e64 s[62:63], 1, v194
	s_andn2_b64 vcc, exec, s[20:21]
	s_barrier
	s_cbranch_vccnz .LBB0_1402
	s_waitcnt lgkmcnt(0)
	v_mfma_f32_16x16x32_bf16 v[60:63], v[130:133], v[186:189], v[60:63]
	v_mfma_f32_16x16x32_bf16 v[56:59], v[138:141], v[186:189], v[56:59]
	v_mfma_f32_16x16x32_bf16 v[44:47], v[130:133], v[178:181], v[44:47]
	v_mfma_f32_16x16x32_bf16 v[40:43], v[138:141], v[178:181], v[40:43]
	v_mfma_f32_16x16x32_bf16 v[28:31], v[130:133], v[170:173], v[28:31]
	v_mfma_f32_16x16x32_bf16 v[24:27], v[138:141], v[170:173], v[24:27]
	v_mfma_f32_16x16x32_bf16 v[12:15], v[130:133], v[162:165], v[12:15]
	v_mfma_f32_16x16x32_bf16 v[8:11], v[138:141], v[162:165], v[8:11]
	v_mfma_f32_16x16x32_bf16 v[60:63], v[134:137], v[190:193], v[60:63]
	v_mfma_f32_16x16x32_bf16 v[56:59], v[142:145], v[190:193], v[56:59]
	v_mfma_f32_16x16x32_bf16 v[44:47], v[134:137], v[182:185], v[44:47]
	v_mfma_f32_16x16x32_bf16 v[40:43], v[142:145], v[182:185], v[40:43]
	v_mfma_f32_16x16x32_bf16 v[28:31], v[134:137], v[174:177], v[28:31]
	v_mfma_f32_16x16x32_bf16 v[24:27], v[142:145], v[174:177], v[24:27]
	v_mfma_f32_16x16x32_bf16 v[12:15], v[134:137], v[166:169], v[12:15]
	v_mfma_f32_16x16x32_bf16 v[8:11], v[142:145], v[166:169], v[8:11]
	v_mfma_f32_16x16x32_bf16 v[52:55], v[146:149], v[186:189], v[52:55]
	v_mfma_f32_16x16x32_bf16 v[48:51], v[154:157], v[186:189], v[48:51]
	v_mfma_f32_16x16x32_bf16 v[36:39], v[146:149], v[178:181], v[36:39]
	v_mfma_f32_16x16x32_bf16 v[32:35], v[154:157], v[178:181], v[32:35]
	v_mfma_f32_16x16x32_bf16 v[20:23], v[146:149], v[170:173], v[20:23]
	v_mfma_f32_16x16x32_bf16 v[16:19], v[154:157], v[170:173], v[16:19]
	v_mfma_f32_16x16x32_bf16 v[4:7], v[146:149], v[162:165], v[4:7]
	v_mfma_f32_16x16x32_bf16 v[0:3], v[154:157], v[162:165], v[0:3]
	v_mfma_f32_16x16x32_bf16 v[52:55], v[150:153], v[190:193], v[52:55]
	v_mfma_f32_16x16x32_bf16 v[48:51], v[158:161], v[190:193], v[48:51]
	v_mfma_f32_16x16x32_bf16 v[36:39], v[150:153], v[182:185], v[36:39]
	v_mfma_f32_16x16x32_bf16 v[32:35], v[158:161], v[182:185], v[32:35]
	v_mfma_f32_16x16x32_bf16 v[20:23], v[150:153], v[174:177], v[20:23]
	v_mfma_f32_16x16x32_bf16 v[16:19], v[158:161], v[174:177], v[16:19]
	v_mfma_f32_16x16x32_bf16 v[4:7], v[150:153], v[166:169], v[4:7]
	v_mfma_f32_16x16x32_bf16 v[0:3], v[158:161], v[166:169], v[0:3]
.LBB0_1402:
	v_mov_b32_e32 v229, v129
	v_lshl_add_u64 v[194:195], s[22:23], 0, v[128:129]
	v_lshl_add_u64 v[196:197], s[22:23], 0, v[228:229]
	s_barrier
	s_add_i32 s2, 0, 0x18000
	v_add_u32_e32 v128, s2, v242
	s_add_i32 s3, 0, 0x1c000
	ds_read_b128 v[146:149], v128
	ds_read_b128 v[150:153], v128 offset:1024
	ds_read_b128 v[154:157], v128 offset:2048
	ds_read_b128 v[158:161], v128 offset:3072
	v_add_u32_e32 v128, s3, v242
	ds_read_b128 v[130:133], v128
	ds_read_b128 v[134:137], v128 offset:1024
	ds_read_b128 v[138:141], v128 offset:2048
	ds_read_b128 v[142:145], v128 offset:3072
	s_mov_b32 m0, s38
	v_cndmask_b32_e64 v128, v212, v244, s[60:61]
	ds_read_b128 v[162:165], v209 offset:32768
	ds_read_b128 v[166:169], v209 offset:33792
	ds_read_b128 v[170:173], v209 offset:34816
	ds_read_b128 v[174:177], v209 offset:35840
	ds_read_b128 v[178:181], v209 offset:36864
	ds_read_b128 v[182:185], v209 offset:37888
	ds_read_b128 v[186:189], v209 offset:38912
	ds_read_b128 v[190:193], v209 offset:39936
	global_load_lds_dwordx4 v128, s[22:23]
	v_cndmask_b32_e64 v128, v214, v245, s[60:61]
	s_mov_b32 m0, s39
	s_nop 0
	global_load_lds_dwordx4 v128, s[22:23]
	s_waitcnt vmcnt(8)
	s_waitcnt lgkmcnt(0)
	s_barrier
	v_mfma_f32_16x16x32_bf16 v[124:127], v[146:149], v[162:165], v[124:127]
	v_mfma_f32_16x16x32_bf16 v[120:123], v[154:157], v[162:165], v[120:123]
	v_mfma_f32_16x16x32_bf16 v[108:111], v[146:149], v[170:173], v[108:111]
	v_mfma_f32_16x16x32_bf16 v[104:107], v[154:157], v[170:173], v[104:107]
	v_mfma_f32_16x16x32_bf16 v[92:95], v[146:149], v[178:181], v[92:95]
	v_mfma_f32_16x16x32_bf16 v[88:91], v[154:157], v[178:181], v[88:91]
	v_mfma_f32_16x16x32_bf16 v[76:79], v[146:149], v[186:189], v[76:79]
	v_mfma_f32_16x16x32_bf16 v[72:75], v[154:157], v[186:189], v[72:75]
	v_mfma_f32_16x16x32_bf16 v[124:127], v[150:153], v[166:169], v[124:127]
	v_mfma_f32_16x16x32_bf16 v[120:123], v[158:161], v[166:169], v[120:123]
	v_mfma_f32_16x16x32_bf16 v[108:111], v[150:153], v[174:177], v[108:111]
	v_mfma_f32_16x16x32_bf16 v[104:107], v[158:161], v[174:177], v[104:107]
	v_mfma_f32_16x16x32_bf16 v[92:95], v[150:153], v[182:185], v[92:95]
	v_mfma_f32_16x16x32_bf16 v[88:91], v[158:161], v[182:185], v[88:91]
	v_mfma_f32_16x16x32_bf16 v[76:79], v[150:153], v[190:193], v[76:79]
	v_mfma_f32_16x16x32_bf16 v[72:75], v[158:161], v[190:193], v[72:75]
	v_mfma_f32_16x16x32_bf16 v[116:119], v[130:133], v[162:165], v[116:119]
	v_mfma_f32_16x16x32_bf16 v[112:115], v[138:141], v[162:165], v[112:115]
	v_mfma_f32_16x16x32_bf16 v[100:103], v[130:133], v[170:173], v[100:103]
	v_mfma_f32_16x16x32_bf16 v[96:99], v[138:141], v[170:173], v[96:99]
	v_mfma_f32_16x16x32_bf16 v[84:87], v[130:133], v[178:181], v[84:87]
	v_mfma_f32_16x16x32_bf16 v[80:83], v[138:141], v[178:181], v[80:83]
	v_mfma_f32_16x16x32_bf16 v[68:71], v[130:133], v[186:189], v[68:71]
	v_mfma_f32_16x16x32_bf16 v[64:67], v[138:141], v[186:189], v[64:67]
	v_mfma_f32_16x16x32_bf16 v[116:119], v[134:137], v[166:169], v[116:119]
	v_mfma_f32_16x16x32_bf16 v[112:115], v[142:145], v[166:169], v[112:115]
	v_mfma_f32_16x16x32_bf16 v[100:103], v[134:137], v[174:177], v[100:103]
	v_mfma_f32_16x16x32_bf16 v[96:99], v[142:145], v[174:177], v[96:99]
	v_mfma_f32_16x16x32_bf16 v[84:87], v[134:137], v[182:185], v[84:87]
	v_mfma_f32_16x16x32_bf16 v[80:83], v[142:145], v[182:185], v[80:83]
	v_mfma_f32_16x16x32_bf16 v[68:71], v[134:137], v[190:193], v[68:71]
	v_mfma_f32_16x16x32_bf16 v[64:67], v[142:145], v[190:193], v[64:67]
	s_barrier
	s_add_i32 s2, s2, s33
	v_lshl_add_u64 v[224:225], v[224:225], 0, s[42:43]
	s_mov_b32 m0, s2
	ds_read_b128 v[186:189], v209 offset:49152
	ds_read_b128 v[190:193], v209 offset:50176
	ds_read_b128 v[178:181], v209 offset:51200
	ds_read_b128 v[182:185], v209 offset:52224
	ds_read_b128 v[170:173], v209 offset:53248
	ds_read_b128 v[174:177], v209 offset:54272
	ds_read_b128 v[162:165], v209 offset:55296
	ds_read_b128 v[166:169], v209 offset:56320
	global_load_lds_dwordx4 v[224:225], off
	v_lshl_add_u64 v[224:225], v[226:227], 0, s[42:43]
	s_add_i32 m0, s2, 0x2000
	v_lshl_add_u64 v[222:223], v[222:223], 0, s[44:45]
	s_add_i32 s2, s3, s33
	global_load_lds_dwordx4 v[224:225], off
	v_lshl_add_u64 v[224:225], v[222:223], 0, v[198:199]
	s_mov_b32 m0, s2
	v_lshl_add_u64 v[222:223], v[222:223], 0, v[200:201]
	global_load_lds_dwordx4 v[224:225], off
	s_add_i32 m0, s2, 0x2000
	v_lshl_add_u64 v[194:195], v[194:195], 0, s[42:43]
	global_load_lds_dwordx4 v[222:223], off
	s_mov_b32 m0, s76
	s_and_b64 vcc, exec, s[62:63]
	global_load_lds_dwordx4 v[194:195], off
	v_lshl_add_u64 v[194:195], v[196:197], 0, s[42:43]
	s_mov_b32 m0, s77
	s_nop 0
	global_load_lds_dwordx4 v[194:195], off
	s_waitcnt vmcnt(8)
	s_waitcnt lgkmcnt(0)
	s_barrier
	s_cbranch_vccnz .LBB0_1399
	s_waitcnt lgkmcnt(0)
	v_mfma_f32_16x16x32_bf16 v[60:63], v[146:149], v[186:189], v[60:63]
	v_mfma_f32_16x16x32_bf16 v[56:59], v[154:157], v[186:189], v[56:59]
	v_mfma_f32_16x16x32_bf16 v[44:47], v[146:149], v[178:181], v[44:47]
	v_mfma_f32_16x16x32_bf16 v[40:43], v[154:157], v[178:181], v[40:43]
	v_mfma_f32_16x16x32_bf16 v[28:31], v[146:149], v[170:173], v[28:31]
	v_mfma_f32_16x16x32_bf16 v[24:27], v[154:157], v[170:173], v[24:27]
	v_mfma_f32_16x16x32_bf16 v[12:15], v[146:149], v[162:165], v[12:15]
	v_mfma_f32_16x16x32_bf16 v[8:11], v[154:157], v[162:165], v[8:11]
	v_mfma_f32_16x16x32_bf16 v[60:63], v[150:153], v[190:193], v[60:63]
	v_mfma_f32_16x16x32_bf16 v[56:59], v[158:161], v[190:193], v[56:59]
	v_mfma_f32_16x16x32_bf16 v[44:47], v[150:153], v[182:185], v[44:47]
	v_mfma_f32_16x16x32_bf16 v[40:43], v[158:161], v[182:185], v[40:43]
	v_mfma_f32_16x16x32_bf16 v[28:31], v[150:153], v[174:177], v[28:31]
	v_mfma_f32_16x16x32_bf16 v[24:27], v[158:161], v[174:177], v[24:27]
	v_mfma_f32_16x16x32_bf16 v[12:15], v[150:153], v[166:169], v[12:15]
	v_mfma_f32_16x16x32_bf16 v[8:11], v[158:161], v[166:169], v[8:11]
	v_mfma_f32_16x16x32_bf16 v[52:55], v[130:133], v[186:189], v[52:55]
	v_mfma_f32_16x16x32_bf16 v[48:51], v[138:141], v[186:189], v[48:51]
	v_mfma_f32_16x16x32_bf16 v[36:39], v[130:133], v[178:181], v[36:39]
	v_mfma_f32_16x16x32_bf16 v[32:35], v[138:141], v[178:181], v[32:35]
	v_mfma_f32_16x16x32_bf16 v[20:23], v[130:133], v[170:173], v[20:23]
	v_mfma_f32_16x16x32_bf16 v[16:19], v[138:141], v[170:173], v[16:19]
	v_mfma_f32_16x16x32_bf16 v[4:7], v[130:133], v[162:165], v[4:7]
	v_mfma_f32_16x16x32_bf16 v[0:3], v[138:141], v[162:165], v[0:3]
	v_mfma_f32_16x16x32_bf16 v[52:55], v[134:137], v[190:193], v[52:55]
	v_mfma_f32_16x16x32_bf16 v[48:51], v[142:145], v[190:193], v[48:51]
	v_mfma_f32_16x16x32_bf16 v[36:39], v[134:137], v[182:185], v[36:39]
	v_mfma_f32_16x16x32_bf16 v[32:35], v[142:145], v[182:185], v[32:35]
	v_mfma_f32_16x16x32_bf16 v[20:23], v[134:137], v[174:177], v[20:23]
	v_mfma_f32_16x16x32_bf16 v[16:19], v[142:145], v[174:177], v[16:19]
	v_mfma_f32_16x16x32_bf16 v[4:7], v[134:137], v[166:169], v[4:7]
	v_mfma_f32_16x16x32_bf16 v[0:3], v[142:145], v[166:169], v[0:3]
	s_branch .LBB0_1399
